# attention block seams: next-block pointer slots read with two ds_read_b32 (they live in LDS) instead of flat loads through the aperture
# baseline (speedup 1.0000x reference)
.Lstg_b8:
	v_mov_b32_e32 v144, s70
	ds_read_b32 v146, v144
	ds_read_b32 v144, v144 offset:4
	s_waitcnt vmcnt(0) lgkmcnt(0)
	v_readfirstlane_b32 s6, v146
	v_readfirstlane_b32 s7, v144
	s_nop 1
	s_nop 3
	s_mov_b32 m0, s81
	s_nop 0
	global_load_lds_dwordx4 v162, s[6:7]
	s_nop 3
	s_add_i32 m0, s78, 0xffffff80
	s_nop 0
	global_load_lds_dwordx4 v162, s[6:7] offset:128
	s_add_i32 m0, s69, 0xffffff00
	s_nop 0
	global_load_lds_dwordx4 v162, s[6:7] offset:256
	s_add_i32 m0, s68, 0xfffffe80
	s_nop 0
	global_load_lds_dwordx4 v162, s[6:7] offset:384
	ds_read_b64_tr_b16 v[144:145], v177 offset:0x8000
	ds_read_b64_tr_b16 v[146:147], v177 offset:0x9000
	ds_read_b64_tr_b16 v[148:149], v177 offset:0xa000
	ds_read_b64_tr_b16 v[150:151], v177 offset:0xb000
	ds_read_b64_tr_b16 v[152:153], v177 offset:0xc000
	ds_read_b64_tr_b16 v[154:155], v177 offset:0xd000
	ds_read_b64_tr_b16 v[156:157], v177 offset:0xe000
	ds_read_b64_tr_b16 v[158:159], v177 offset:0xf000
	ds_read_b64_tr_b16 v[166:167], v177 offset:0x8200
	ds_read_b64_tr_b16 v[168:169], v177 offset:0x9200
	ds_read_b64_tr_b16 v[170:171], v177 offset:0xa200
	ds_read_b64_tr_b16 v[172:173], v177 offset:0xb200
	ds_read_b64_tr_b16 v[180:181], v177 offset:0xc200
	ds_read_b64_tr_b16 v[182:183], v177 offset:0xd200
	ds_read_b64_tr_b16 v[184:185], v177 offset:0xe200
	ds_read_b64_tr_b16 v[186:187], v177 offset:0xf200
	s_waitcnt lgkmcnt(8)
	s_nop 1
	v_mfma_f32_32x32x16_bf16 v[112:127], v[144:147], v[128:131], v[112:127]
	v_mfma_f32_32x32x16_bf16 v[112:127], v[148:151], v[132:135], v[112:127]
	v_mfma_f32_32x32x16_bf16 v[112:127], v[152:155], v[136:139], v[112:127]
	v_mfma_f32_32x32x16_bf16 v[112:127], v[156:159], v[140:143], v[112:127]
	ds_read_b64_tr_b16 v[144:145], v177 offset:0x8400
	ds_read_b64_tr_b16 v[146:147], v177 offset:0x9400
	ds_read_b64_tr_b16 v[148:149], v177 offset:0xa400
	ds_read_b64_tr_b16 v[150:151], v177 offset:0xb400
	ds_read_b64_tr_b16 v[152:153], v177 offset:0xc400
	ds_read_b64_tr_b16 v[154:155], v177 offset:0xd400
	ds_read_b64_tr_b16 v[156:157], v177 offset:0xe400
	ds_read_b64_tr_b16 v[158:159], v177 offset:0xf400
	s_waitcnt lgkmcnt(8)
	v_mfma_f32_32x32x16_bf16 v[0:15], v[166:169], v[128:131], v[0:15]
	v_mfma_f32_32x32x16_bf16 v[0:15], v[170:173], v[132:135], v[0:15]
	v_mfma_f32_32x32x16_bf16 v[0:15], v[180:183], v[136:139], v[0:15]
	v_mfma_f32_32x32x16_bf16 v[0:15], v[184:187], v[140:143], v[0:15]
	ds_read_b64_tr_b16 v[166:167], v177 offset:0x8600
	ds_read_b64_tr_b16 v[168:169], v177 offset:0x9600
	ds_read_b64_tr_b16 v[170:171], v177 offset:0xa600
	ds_read_b64_tr_b16 v[172:173], v177 offset:0xb600
	ds_read_b64_tr_b16 v[180:181], v177 offset:0xc600
	ds_read_b64_tr_b16 v[182:183], v177 offset:0xd600
	ds_read_b64_tr_b16 v[184:185], v177 offset:0xe600
	ds_read_b64_tr_b16 v[186:187], v177 offset:0xf600
	s_waitcnt lgkmcnt(8)
	v_mfma_f32_32x32x16_bf16 v[16:31], v[144:147], v[128:131], v[16:31]
	v_mfma_f32_32x32x16_bf16 v[16:31], v[148:151], v[132:135], v[16:31]
	v_mfma_f32_32x32x16_bf16 v[16:31], v[152:155], v[136:139], v[16:31]
	v_mfma_f32_32x32x16_bf16 v[16:31], v[156:159], v[140:143], v[16:31]
	ds_read_b64_tr_b16 v[144:145], v177 offset:0x8800
	ds_read_b64_tr_b16 v[146:147], v177 offset:0x9800
	ds_read_b64_tr_b16 v[148:149], v177 offset:0xa800
	ds_read_b64_tr_b16 v[150:151], v177 offset:0xb800
	ds_read_b64_tr_b16 v[152:153], v177 offset:0xc800
	ds_read_b64_tr_b16 v[154:155], v177 offset:0xd800
	ds_read_b64_tr_b16 v[156:157], v177 offset:0xe800
	ds_read_b64_tr_b16 v[158:159], v177 offset:0xf800
	s_waitcnt lgkmcnt(8)
	v_mfma_f32_32x32x16_bf16 v[32:47], v[166:169], v[128:131], v[32:47]
	v_mfma_f32_32x32x16_bf16 v[32:47], v[170:173], v[132:135], v[32:47]
	v_mfma_f32_32x32x16_bf16 v[32:47], v[180:183], v[136:139], v[32:47]
	v_mfma_f32_32x32x16_bf16 v[32:47], v[184:187], v[140:143], v[32:47]
	ds_read_b64_tr_b16 v[166:167], v177 offset:0x8a00
	ds_read_b64_tr_b16 v[168:169], v177 offset:0x9a00
	ds_read_b64_tr_b16 v[170:171], v177 offset:0xaa00
	ds_read_b64_tr_b16 v[172:173], v177 offset:0xba00
	ds_read_b64_tr_b16 v[180:181], v177 offset:0xca00
	ds_read_b64_tr_b16 v[182:183], v177 offset:0xda00
	ds_read_b64_tr_b16 v[184:185], v177 offset:0xea00
	ds_read_b64_tr_b16 v[186:187], v177 offset:0xfa00
	s_waitcnt lgkmcnt(8)
	v_mfma_f32_32x32x16_bf16 v[48:63], v[144:147], v[128:131], v[48:63]
	v_mfma_f32_32x32x16_bf16 v[48:63], v[148:151], v[132:135], v[48:63]
	v_mfma_f32_32x32x16_bf16 v[48:63], v[152:155], v[136:139], v[48:63]
	v_mfma_f32_32x32x16_bf16 v[48:63], v[156:159], v[140:143], v[48:63]
	ds_read_b64_tr_b16 v[144:145], v177 offset:0x8c00
	ds_read_b64_tr_b16 v[146:147], v177 offset:0x9c00
	ds_read_b64_tr_b16 v[148:149], v177 offset:0xac00
	ds_read_b64_tr_b16 v[150:151], v177 offset:0xbc00
	ds_read_b64_tr_b16 v[152:153], v177 offset:0xcc00
	ds_read_b64_tr_b16 v[154:155], v177 offset:0xdc00
	ds_read_b64_tr_b16 v[156:157], v177 offset:0xec00
	ds_read_b64_tr_b16 v[158:159], v177 offset:0xfc00
	s_waitcnt lgkmcnt(8)
	v_mfma_f32_32x32x16_bf16 v[64:79], v[166:169], v[128:131], v[64:79]
	v_mfma_f32_32x32x16_bf16 v[64:79], v[170:173], v[132:135], v[64:79]
	v_mfma_f32_32x32x16_bf16 v[64:79], v[180:183], v[136:139], v[64:79]
	v_mfma_f32_32x32x16_bf16 v[64:79], v[184:187], v[140:143], v[64:79]
	ds_read_b64_tr_b16 v[166:167], v177 offset:0x8e00
	ds_read_b64_tr_b16 v[168:169], v177 offset:0x9e00
	ds_read_b64_tr_b16 v[170:171], v177 offset:0xae00
	ds_read_b64_tr_b16 v[172:173], v177 offset:0xbe00
	ds_read_b64_tr_b16 v[180:181], v177 offset:0xce00
	ds_read_b64_tr_b16 v[182:183], v177 offset:0xde00
	ds_read_b64_tr_b16 v[184:185], v177 offset:0xee00
	ds_read_b64_tr_b16 v[186:187], v177 offset:0xfe00
	s_waitcnt lgkmcnt(8)
	v_mfma_f32_32x32x16_bf16 v[80:95], v[144:147], v[128:131], v[80:95]
	v_mfma_f32_32x32x16_bf16 v[80:95], v[148:151], v[132:135], v[80:95]
	v_mfma_f32_32x32x16_bf16 v[80:95], v[152:155], v[136:139], v[80:95]
	v_mfma_f32_32x32x16_bf16 v[80:95], v[156:159], v[140:143], v[80:95]
	s_waitcnt lgkmcnt(0)
	v_mfma_f32_32x32x16_bf16 v[96:111], v[166:169], v[128:131], v[96:111]
	v_mfma_f32_32x32x16_bf16 v[96:111], v[170:173], v[132:135], v[96:111]
	v_mfma_f32_32x32x16_bf16 v[96:111], v[180:183], v[136:139], v[96:111]
	v_mfma_f32_32x32x16_bf16 v[96:111], v[184:187], v[140:143], v[96:111]
	v_readlane_b32 s6, v255, 31
	v_readlane_b32 s7, v255, 32
	v_readlane_b32 s12, v255, 49
	v_readlane_b32 s13, v255, 50
	v_mov_b64_e32 v[128:129], s[6:7]
	v_readlane_b32 s6, v255, 35
	v_readlane_b32 s7, v255, 36
	flat_load_dword v130, v[128:129] sc0 sc1
	s_waitcnt vmcnt(0)
	s_ashr_i32 s13, s12, 31
	v_mov_b64_e32 v[128:129], s[6:7]
	flat_load_dword v131, v[128:129] sc0 sc1
	s_waitcnt vmcnt(0)
	s_lshl_b64 s[6:7], s[12:13], 11
	v_lshl_or_b32 v128, v175, 11, v174
	v_mov_b32_e32 v129, v161
	s_waitcnt lgkmcnt(0)
	s_barrier
	v_add_f32_e32 v158, v179, v204
	s_waitcnt lgkmcnt(0)
	v_readfirstlane_b32 s9, v130
	s_add_u32 s6, s9, s6
	v_readfirstlane_b32 s8, v131
	s_addc_u32 s7, s8, s7
	v_lshl_add_u64 v[156:157], s[6:7], 0, v[128:129]
	flat_load_dwordx4 v[128:131], v[156:157]
	flat_load_dwordx4 v[132:135], v[156:157] offset:32
	flat_load_dwordx4 v[136:139], v[156:157] offset:64
	flat_load_dwordx4 v[140:143], v[156:157] offset:96
	flat_load_dwordx4 v[144:147], v[156:157] offset:128
	flat_load_dwordx4 v[148:151], v[156:157] offset:160
	flat_load_dwordx4 v[152:155], v[156:157] offset:192
	flat_load_dwordx4 v[166:169], v[156:157] offset:224
	v_readlane_b32 s6, v255, 51
	v_readlane_b32 s7, v255, 52
	s_add_u32 s4, s4, s6
	s_addc_u32 s5, s5, s7
	v_lshl_add_u64 v[156:157], s[4:5], 0, v[160:161]
	flat_load_dword v156, v[156:157]
	v_mov_b32_e32 v157, v158
	s_nop 1
	v_permlane32_swap_b32_e32 v158, v157
	v_add_f32_e32 v157, v158, v157
	s_mul_i32 s5, s12, 0x6800
	s_mul_hi_i32 s4, s12, 0x6800
	s_add_u32 s2, s2, s5
	s_addc_u32 s3, s3, s4
	s_add_u32 s4, s2, 0x1000
	s_addc_u32 s5, s3, 0
	v_readlane_b32 s2, v255, 27
	s_waitcnt vmcnt(0) lgkmcnt(0)
	v_max_f32_e32 v156, v156, v156
	v_max_f32_e64 v156, |v157|, v156
	v_rcp_f32_e32 v194, v156
	s_nop 0
	v_mul_f32_e32 v196, v113, v194
	v_mul_f32_e32 v213, v115, v194
	v_mul_f32_e32 v195, v112, v194
	v_mul_f32_e32 v197, v114, v194
	v_mul_f32_e32 v217, v119, v194
	v_mul_f32_e32 v119, v52, v194
	v_mul_f32_e32 v115, v54, v194
	v_mul_f32_e32 v54, v56, v194
	v_mul_f32_e32 v52, v57, v194
	v_mul_f32_e32 v56, v196, v196
	v_mul_f32_e32 v57, v213, v213
	v_mul_f32_e32 v215, v117, v194
	v_fmac_f32_e32 v56, v195, v195
	v_fmac_f32_e32 v57, v197, v197
	v_mul_f32_e32 v214, v116, v194
	v_mul_f32_e32 v216, v118, v194
	v_mul_f32_e32 v114, v50, v194
	v_mul_f32_e32 v50, v58, v194
	v_add_f32_e32 v56, v56, v57
	v_mul_f32_e32 v57, v215, v215
	v_mul_f32_e32 v58, v217, v217
	v_mul_f32_e32 v219, v121, v194
	v_mul_f32_e32 v210, v123, v194
	v_fmac_f32_e32 v57, v214, v214
	v_fmac_f32_e32 v58, v216, v216
	v_mul_f32_e32 v218, v120, v194
	v_mul_f32_e32 v212, v122, v194
	v_mul_f32_e32 v118, v48, v194
	v_mul_f32_e32 v48, v59, v194
	v_add_f32_e32 v57, v57, v58
	v_mul_f32_e32 v58, v219, v219
	v_mul_f32_e32 v59, v210, v210
	v_mul_f32_e32 v221, v125, v194
	v_mul_f32_e32 v211, v127, v194
	v_fmac_f32_e32 v58, v218, v218
	v_fmac_f32_e32 v59, v212, v212
	v_mul_f32_e32 v220, v124, v194
	v_mul_f32_e32 v222, v126, v194
	v_mul_f32_e32 v113, v55, v194
	v_mul_f32_e32 v55, v60, v194
	v_add_f32_e32 v58, v58, v59
	v_mul_f32_e32 v59, v221, v221
	v_mul_f32_e32 v60, v211, v211
	v_fmac_f32_e32 v59, v220, v220
	v_fmac_f32_e32 v60, v222, v222
	v_add_f32_e32 v59, v59, v60
	v_mul_f32_e32 v206, v1, v194
	v_mul_f32_e32 v202, v3, v194
	v_add_f32_e32 v56, v56, v57
	v_add_f32_e32 v57, v58, v59
	v_mul_f32_e32 v208, v0, v194
	v_mul_f32_e32 v204, v2, v194
	v_add_f32_e32 v56, v56, v57
	v_mul_f32_e32 v57, v206, v206
	v_mul_f32_e32 v58, v202, v202
	v_mul_f32_e32 v207, v5, v194
	v_mul_f32_e32 v203, v7, v194
	v_fmac_f32_e32 v57, v208, v208
	v_fmac_f32_e32 v58, v204, v204
	v_mul_f32_e32 v209, v4, v194
	v_mul_f32_e32 v205, v6, v194
	v_add_f32_e32 v57, v57, v58
	v_mul_f32_e32 v58, v207, v207
	v_mul_f32_e32 v59, v203, v203
	v_mul_f32_e32 v198, v9, v194
	v_mul_f32_e32 v190, v11, v194
	v_fmac_f32_e32 v58, v209, v209
	v_fmac_f32_e32 v59, v205, v205
	v_mul_f32_e32 v200, v8, v194
	v_mul_f32_e32 v192, v10, v194
	v_add_f32_e32 v58, v58, v59
	v_mul_f32_e32 v59, v198, v198
	v_mul_f32_e32 v60, v190, v190
	v_mul_f32_e32 v199, v13, v194
	v_mul_f32_e32 v191, v15, v194
	v_fmac_f32_e32 v59, v200, v200
	v_fmac_f32_e32 v60, v192, v192
	v_mul_f32_e32 v201, v12, v194
	v_mul_f32_e32 v193, v14, v194
	v_mul_f32_e32 v117, v53, v194
	v_mul_f32_e32 v53, v61, v194
	v_add_f32_e32 v59, v59, v60
	v_mul_f32_e32 v60, v199, v199
	v_mul_f32_e32 v61, v191, v191
	v_fmac_f32_e32 v60, v201, v201
	v_fmac_f32_e32 v61, v193, v193
	v_add_f32_e32 v60, v60, v61
	v_add_f32_e32 v57, v57, v58
	v_add_f32_e32 v58, v59, v60
	v_mul_f32_e32 v186, v17, v194
	v_mul_f32_e32 v182, v19, v194
	v_add_f32_e32 v57, v57, v58
	v_mul_f32_e32 v188, v16, v194
	v_mul_f32_e32 v184, v18, v194
	v_add_f32_e32 v56, v56, v57
	v_mul_f32_e32 v57, v186, v186
	v_mul_f32_e32 v58, v182, v182
	v_mul_f32_e32 v187, v21, v194
	v_mul_f32_e32 v183, v23, v194
	v_fmac_f32_e32 v57, v188, v188
	v_fmac_f32_e32 v58, v184, v184
	v_mul_f32_e32 v189, v20, v194
	v_mul_f32_e32 v185, v22, v194
	v_add_f32_e32 v57, v57, v58
	v_mul_f32_e32 v58, v187, v187
	v_mul_f32_e32 v59, v183, v183
	v_mul_f32_e32 v178, v25, v194
	v_mul_f32_e32 v171, v27, v194
	v_fmac_f32_e32 v58, v189, v189
	v_fmac_f32_e32 v59, v185, v185
	v_mul_f32_e32 v180, v24, v194
	v_mul_f32_e32 v173, v26, v194
	v_add_f32_e32 v58, v58, v59
	v_mul_f32_e32 v59, v178, v178
	v_mul_f32_e32 v60, v171, v171
	v_mul_f32_e32 v179, v29, v194
	v_mul_f32_e32 v172, v31, v194
	v_fmac_f32_e32 v59, v180, v180
	v_fmac_f32_e32 v60, v173, v173
	v_mul_f32_e32 v181, v28, v194
	v_mul_f32_e32 v177, v30, v194
	v_add_f32_e32 v59, v59, v60
	v_mul_f32_e32 v60, v179, v179
	v_mul_f32_e32 v61, v172, v172
	v_fmac_f32_e32 v60, v181, v181
	v_fmac_f32_e32 v61, v177, v177
	v_add_f32_e32 v60, v60, v61
	v_add_f32_e32 v57, v57, v58
	v_add_f32_e32 v58, v59, v60
	v_mul_f32_e32 v160, v33, v194
	v_mul_f32_e32 v156, v35, v194
	v_add_f32_e32 v57, v57, v58
	v_mul_f32_e32 v163, v32, v194
	v_mul_f32_e32 v158, v34, v194
	v_add_f32_e32 v56, v57, v56
	v_mul_f32_e32 v57, v160, v160
	v_mul_f32_e32 v58, v156, v156
	v_mul_f32_e32 v162, v37, v194
	v_mul_f32_e32 v157, v39, v194
	v_fmac_f32_e32 v57, v163, v163
	v_fmac_f32_e32 v58, v158, v158
	v_mul_f32_e32 v170, v36, v194
	v_mul_f32_e32 v159, v38, v194
	v_add_f32_e32 v57, v57, v58
	v_mul_f32_e32 v58, v162, v162
	v_mul_f32_e32 v59, v157, v157
	v_mul_f32_e32 v124, v41, v194
	v_mul_f32_e32 v120, v43, v194
	v_fmac_f32_e32 v58, v170, v170
	v_fmac_f32_e32 v59, v159, v159
	v_mul_f32_e32 v126, v40, v194
	v_mul_f32_e32 v122, v42, v194
	v_add_f32_e32 v58, v58, v59
	v_mul_f32_e32 v59, v124, v124
	v_mul_f32_e32 v60, v120, v120
	v_mul_f32_e32 v125, v45, v194
	v_mul_f32_e32 v121, v47, v194
	v_fmac_f32_e32 v59, v126, v126
	v_fmac_f32_e32 v60, v122, v122
	v_mul_f32_e32 v127, v44, v194
	v_mul_f32_e32 v123, v46, v194
	v_add_f32_e32 v59, v59, v60
	v_mul_f32_e32 v60, v125, v125
	v_mul_f32_e32 v61, v121, v121
	v_fmac_f32_e32 v60, v127, v127
	v_fmac_f32_e32 v61, v123, v123
	v_add_f32_e32 v60, v60, v61
	v_add_f32_e32 v57, v57, v58
	v_add_f32_e32 v58, v59, v60
	v_mul_f32_e32 v116, v49, v194
	v_mul_f32_e32 v112, v51, v194
	v_add_f32_e32 v57, v57, v58
	v_add_f32_e32 v56, v57, v56
	v_mul_f32_e32 v57, v116, v116
	v_mul_f32_e32 v58, v112, v112
	v_fmac_f32_e32 v57, v118, v118
	v_fmac_f32_e32 v58, v114, v114
	v_add_f32_e32 v57, v57, v58
	v_mul_f32_e32 v58, v117, v117
	v_mul_f32_e32 v59, v113, v113
	v_fmac_f32_e32 v58, v119, v119
	v_fmac_f32_e32 v59, v115, v115
	v_add_f32_e32 v58, v58, v59
	v_mul_f32_e32 v59, v52, v52
	v_mul_f32_e32 v60, v48, v48
	v_mul_f32_e32 v49, v63, v194
	v_fmac_f32_e32 v59, v54, v54
	v_fmac_f32_e32 v60, v50, v50
	v_mul_f32_e32 v51, v62, v194
	v_add_f32_e32 v59, v59, v60
	v_mul_f32_e32 v60, v53, v53
	v_mul_f32_e32 v61, v49, v49
	v_fmac_f32_e32 v60, v55, v55
	v_fmac_f32_e32 v61, v51, v51
	v_add_f32_e32 v60, v60, v61
	v_add_f32_e32 v57, v57, v58
	v_add_f32_e32 v58, v59, v60
	v_mul_f32_e32 v44, v65, v194
	v_mul_f32_e32 v40, v67, v194
	v_add_f32_e32 v57, v57, v58
	v_mul_f32_e32 v46, v64, v194
	v_mul_f32_e32 v42, v66, v194
	v_add_f32_e32 v56, v57, v56
	v_mul_f32_e32 v57, v44, v44
	v_mul_f32_e32 v58, v40, v40
	v_mul_f32_e32 v45, v69, v194
	v_mul_f32_e32 v41, v71, v194
	v_fmac_f32_e32 v57, v46, v46
	v_fmac_f32_e32 v58, v42, v42
	v_mul_f32_e32 v47, v68, v194
	v_mul_f32_e32 v43, v70, v194
	v_add_f32_e32 v57, v57, v58
	v_mul_f32_e32 v58, v45, v45
	v_mul_f32_e32 v59, v41, v41
	v_mul_f32_e32 v36, v73, v194
	v_mul_f32_e32 v32, v75, v194
	v_fmac_f32_e32 v58, v47, v47
	v_fmac_f32_e32 v59, v43, v43
	v_mul_f32_e32 v38, v72, v194
	v_mul_f32_e32 v34, v74, v194
	v_add_f32_e32 v58, v58, v59
	v_mul_f32_e32 v59, v36, v36
	v_mul_f32_e32 v60, v32, v32
	v_mul_f32_e32 v37, v77, v194
	v_mul_f32_e32 v33, v79, v194
	v_fmac_f32_e32 v59, v38, v38
	v_fmac_f32_e32 v60, v34, v34
	v_mul_f32_e32 v39, v76, v194
	v_mul_f32_e32 v35, v78, v194
	v_add_f32_e32 v59, v59, v60
	v_mul_f32_e32 v60, v37, v37
	v_mul_f32_e32 v61, v33, v33
	v_fmac_f32_e32 v60, v39, v39
	v_fmac_f32_e32 v61, v35, v35
	v_mul_f32_e32 v31, v84, v194
	v_add_f32_e32 v60, v60, v61
	v_mul_u32_u24_e32 v84, 0x6800, v175
	v_add_f32_e32 v57, v57, v58
	v_add_f32_e32 v58, v59, v60
	v_lshl_or_b32 v59, v176, 3, v84
	global_load_dwordx2 v[68:69], v59, s[4:5]
	global_load_dwordx2 v[70:71], v59, s[4:5] offset:16
	global_load_dwordx2 v[72:73], v59, s[4:5] offset:32
	global_load_dwordx2 v[74:75], v59, s[4:5] offset:48
	v_mul_f32_e32 v30, v80, v194
	v_mul_f32_e32 v28, v81, v194
	v_mul_f32_e32 v26, v82, v194
	v_mul_f32_e32 v24, v83, v194
	v_add_f32_e32 v57, v57, v58
	global_load_dwordx2 v[76:77], v59, s[4:5] offset:64
	global_load_dwordx2 v[78:79], v59, s[4:5] offset:80
	global_load_dwordx2 v[80:81], v59, s[4:5] offset:96
	global_load_dwordx2 v[82:83], v59, s[4:5] offset:112
	v_add_f32_e32 v56, v57, v56
	v_mul_f32_e32 v57, v28, v28
	v_mul_f32_e32 v58, v24, v24
	v_mul_f32_e32 v29, v85, v194
	v_mul_f32_e32 v25, v87, v194
	v_fmac_f32_e32 v57, v30, v30
	v_fmac_f32_e32 v58, v26, v26
	v_mul_f32_e32 v27, v86, v194
	v_add_f32_e32 v57, v57, v58
	v_mul_f32_e32 v58, v29, v29
	v_mul_f32_e32 v60, v25, v25
	v_mul_f32_e32 v20, v89, v194
	v_mul_f32_e32 v16, v91, v194
	v_fmac_f32_e32 v58, v31, v31
	v_fmac_f32_e32 v60, v27, v27
	v_mul_f32_e32 v22, v88, v194
	v_mul_f32_e32 v18, v90, v194
	v_add_f32_e32 v58, v58, v60
	v_mul_f32_e32 v60, v20, v20
	v_mul_f32_e32 v61, v16, v16
	v_mul_f32_e32 v21, v93, v194
	v_mul_f32_e32 v17, v95, v194
	v_fmac_f32_e32 v60, v22, v22
	v_fmac_f32_e32 v61, v18, v18
	v_mul_f32_e32 v23, v92, v194
	v_mul_f32_e32 v19, v94, v194
	v_add_f32_e32 v60, v60, v61
	v_mul_f32_e32 v61, v21, v21
	v_mul_f32_e32 v62, v17, v17
	v_fmac_f32_e32 v61, v23, v23
	v_fmac_f32_e32 v62, v19, v19
	v_add_f32_e32 v61, v61, v62
	v_add_f32_e32 v57, v57, v58
	v_add_f32_e32 v58, v60, v61
	v_mul_f32_e32 v12, v97, v194
	v_mul_f32_e32 v8, v99, v194
	v_add_f32_e32 v57, v57, v58
	v_mul_f32_e32 v14, v96, v194
	v_mul_f32_e32 v10, v98, v194
	v_add_f32_e32 v56, v57, v56
	v_mul_f32_e32 v57, v12, v12
	v_mul_f32_e32 v58, v8, v8
	v_mul_f32_e32 v13, v101, v194
	v_mul_f32_e32 v9, v103, v194
	v_fmac_f32_e32 v57, v14, v14
	v_fmac_f32_e32 v58, v10, v10
	v_mul_f32_e32 v15, v100, v194
	v_mul_f32_e32 v11, v102, v194
	v_add_f32_e32 v57, v57, v58
	v_mul_f32_e32 v58, v13, v13
	v_mul_f32_e32 v60, v9, v9
	v_mul_f32_e32 v4, v105, v194
	v_mul_f32_e32 v0, v107, v194
	v_fmac_f32_e32 v58, v15, v15
	v_fmac_f32_e32 v60, v11, v11
	v_mul_f32_e32 v6, v104, v194
	v_mul_f32_e32 v2, v106, v194
	v_add_f32_e32 v58, v58, v60
	v_mul_f32_e32 v60, v4, v4
	v_mul_f32_e32 v61, v0, v0
	v_mul_f32_e32 v5, v109, v194
	v_mul_f32_e32 v1, v111, v194
	v_fmac_f32_e32 v60, v6, v6
	v_fmac_f32_e32 v61, v2, v2
	v_mul_f32_e32 v7, v108, v194
	v_mul_f32_e32 v3, v110, v194
	v_add_f32_e32 v60, v60, v61
	v_mul_f32_e32 v61, v5, v5
	v_mul_f32_e32 v62, v1, v1
	v_fmac_f32_e32 v61, v7, v7
	v_fmac_f32_e32 v62, v3, v3
	v_add_f32_e32 v61, v61, v62
	v_add_f32_e32 v57, v57, v58
	v_add_f32_e32 v58, v60, v61
	v_add_f32_e32 v57, v57, v58
	v_add_f32_e32 v56, v57, v56
	v_mov_b32_e32 v57, v56
	s_nop 1
	v_permlane32_swap_b32_e32 v56, v57
	v_add_f32_e32 v56, v56, v57
	v_fmamk_f32 v56, v56, 0x3b800000, v254
	v_rsq_f32_e32 v56, v56
	v_add_u32_e32 v57, s2, v174
	ds_read_b128 v[60:63], v57
	ds_read_b128 v[64:67], v57 offset:32
	v_mul_f32_e32 v58, v195, v56
	v_mul_f32_e32 v54, v54, v56
	v_mul_f32_e32 v52, v52, v56
	s_waitcnt lgkmcnt(1)
	v_mul_f32_e32 v58, v58, v60
	v_mul_f32_e32 v60, v214, v56
	s_waitcnt lgkmcnt(0)
	v_mul_f32_e32 v60, v60, v64
	v_mul_f32_e32 v64, v196, v56
	v_mul_f32_e32 v61, v64, v61
	v_mul_f32_e32 v64, v215, v56
	v_mul_f32_e32 v64, v64, v65
	v_mul_f32_e32 v65, v197, v56
	v_mul_f32_e32 v62, v65, v62
	v_mul_f32_e32 v65, v216, v56
	v_mul_f32_e32 v65, v65, v66
	v_mul_f32_e32 v66, v213, v56
	v_mul_f32_e32 v63, v66, v63
	v_mul_f32_e32 v66, v217, v56
	v_mul_f32_e32 v66, v66, v67
	s_waitcnt vmcnt(7)
	v_lshlrev_b32_e32 v67, 16, v68
	v_mul_f32_e32 v58, v58, v67
	v_and_b32_e32 v67, 0xffff0000, v68
	v_mul_f32_e32 v61, v61, v67
	v_lshlrev_b32_e32 v67, 16, v69
	v_mul_f32_e32 v62, v62, v67
	v_and_b32_e32 v67, 0xffff0000, v69
	v_mul_f32_e32 v63, v63, v67
	s_waitcnt vmcnt(6)
	v_lshlrev_b32_e32 v67, 16, v70
	v_mul_f32_e32 v67, v60, v67
	v_and_b32_e32 v60, 0xffff0000, v70
	v_mul_f32_e32 v64, v64, v60
	v_lshlrev_b32_e32 v60, 16, v71
	v_mul_f32_e32 v65, v65, v60
	v_and_b32_e32 v60, 0xffff0000, v71
	v_mul_f32_e32 v66, v66, v60
	v_cvt_pk_bf16_f32 v60, v58, v61
	v_cvt_pk_bf16_f32 v61, v62, v63
	v_cvt_pk_bf16_f32 v62, v67, v64
	v_cvt_pk_bf16_f32 v63, v65, v66
	ds_read_b128 v[64:67], v57 offset:64
	ds_read_b128 v[68:71], v57 offset:96
	v_permlane32_swap_b32_e32 v60, v62
	v_permlane32_swap_b32_e32 v61, v63
	v_or_b32_e32 v58, v174, v84
	global_store_dwordx4 v58, v[60:63], s[4:5]
	v_mul_f32_e32 v50, v50, v56
	v_mul_f32_e32 v48, v48, v56
	v_mul_f32_e32 v60, v218, v56
	v_mul_f32_e32 v61, v220, v56
	s_waitcnt lgkmcnt(1)
	v_mul_f32_e32 v60, v60, v64
	s_waitcnt lgkmcnt(0)
	v_mul_f32_e32 v61, v61, v68
	v_mul_f32_e32 v62, v219, v56
	s_waitcnt vmcnt(6)
	v_lshlrev_b32_e32 v68, 16, v72
	v_mul_f32_e32 v62, v62, v65
	v_mul_f32_e32 v64, v212, v56
	v_mul_f32_e32 v60, v60, v68
	v_and_b32_e32 v68, 0xffff0000, v72
	v_mul_f32_e32 v64, v64, v66
	v_mul_f32_e32 v66, v210, v56
	v_mul_f32_e32 v62, v62, v68
	v_lshlrev_b32_e32 v68, 16, v73
	v_mul_f32_e32 v66, v66, v67
	v_mul_f32_e32 v64, v64, v68
	v_and_b32_e32 v68, 0xffff0000, v73
	v_mul_f32_e32 v63, v221, v56
	v_mul_f32_e32 v66, v66, v68
	s_waitcnt vmcnt(5)
	v_lshlrev_b32_e32 v68, 16, v74
	v_mul_f32_e32 v63, v63, v69
	v_mul_f32_e32 v65, v222, v56
	v_mul_f32_e32 v68, v61, v68
	v_and_b32_e32 v61, 0xffff0000, v74
	v_mul_f32_e32 v65, v65, v70
	v_mul_f32_e32 v67, v211, v56
	v_mul_f32_e32 v63, v63, v61
	v_lshlrev_b32_e32 v61, 16, v75
	v_mul_f32_e32 v67, v67, v71
	v_mul_f32_e32 v65, v65, v61
	v_and_b32_e32 v61, 0xffff0000, v75
	v_mul_f32_e32 v67, v67, v61
	v_cvt_pk_bf16_f32 v60, v60, v62
	v_cvt_pk_bf16_f32 v61, v64, v66
	v_cvt_pk_bf16_f32 v62, v68, v63
	v_cvt_pk_bf16_f32 v63, v65, v67
	v_mul_f32_e32 v68, v208, v56
	v_permlane32_swap_b32_e32 v60, v62
	v_permlane32_swap_b32_e32 v61, v63
	global_store_dwordx4 v58, v[60:63], s[4:5] offset:32
	global_load_dwordx2 v[72:73], v59, s[4:5] offset:128
	global_load_dwordx2 v[74:75], v59, s[4:5] offset:144
	global_load_dwordx2 v[84:85], v59, s[4:5] offset:160
	global_load_dwordx2 v[86:87], v59, s[4:5] offset:176
	ds_read_b128 v[60:63], v57 offset:128
	ds_read_b128 v[64:67], v57 offset:160
	v_mul_f32_e32 v55, v55, v56
	v_mul_f32_e32 v53, v53, v56
	v_mul_f32_e32 v51, v51, v56
	s_waitcnt lgkmcnt(1)
	v_mul_f32_e32 v60, v68, v60
	v_mul_f32_e32 v68, v209, v56
	s_waitcnt lgkmcnt(0)
	v_mul_f32_e32 v64, v68, v64
	v_mul_f32_e32 v68, v206, v56
	v_mul_f32_e32 v61, v68, v61
	v_mul_f32_e32 v68, v207, v56
	v_mul_f32_e32 v65, v68, v65
	v_mul_f32_e32 v68, v204, v56
	v_mul_f32_e32 v62, v68, v62
	v_mul_f32_e32 v68, v205, v56
	v_mul_f32_e32 v66, v68, v66
	v_mul_f32_e32 v68, v202, v56
	v_mul_f32_e32 v63, v68, v63
	v_mul_f32_e32 v68, v203, v56
	v_mul_f32_e32 v67, v68, v67
	s_waitcnt vmcnt(9)
	v_lshlrev_b32_e32 v68, 16, v76
	v_mul_f32_e32 v60, v60, v68
	v_and_b32_e32 v68, 0xffff0000, v76
	v_mul_f32_e32 v61, v61, v68
	v_lshlrev_b32_e32 v68, 16, v77
	v_mul_f32_e32 v62, v62, v68
	v_and_b32_e32 v68, 0xffff0000, v77
	v_mul_f32_e32 v63, v63, v68
	s_waitcnt vmcnt(8)
	v_lshlrev_b32_e32 v68, 16, v78
	v_mul_f32_e32 v64, v64, v68
	v_and_b32_e32 v68, 0xffff0000, v78
	v_mul_f32_e32 v65, v65, v68
	v_lshlrev_b32_e32 v68, 16, v79
	v_mul_f32_e32 v66, v66, v68
	v_and_b32_e32 v68, 0xffff0000, v79
	v_mul_f32_e32 v67, v67, v68
	v_cvt_pk_bf16_f32 v60, v60, v61
	v_cvt_pk_bf16_f32 v61, v62, v63
	v_cvt_pk_bf16_f32 v62, v64, v65
	v_cvt_pk_bf16_f32 v63, v66, v67
	ds_read_b128 v[64:67], v57 offset:192
	ds_read_b128 v[68:71], v57 offset:224
	v_permlane32_swap_b32_e32 v60, v62
	v_permlane32_swap_b32_e32 v61, v63
	global_store_dwordx4 v58, v[60:63], s[4:5] offset:64
	v_mul_f32_e32 v49, v49, v56
	v_mul_f32_e32 v46, v46, v56
	v_mul_f32_e32 v60, v200, v56
	v_mul_f32_e32 v61, v201, v56
	s_waitcnt lgkmcnt(1)
	v_mul_f32_e32 v60, v60, v64
	s_waitcnt lgkmcnt(0)
	v_mul_f32_e32 v61, v61, v68
	v_mul_f32_e32 v62, v198, v56
	s_waitcnt vmcnt(8)
	v_lshlrev_b32_e32 v68, 16, v80
	v_mul_f32_e32 v62, v62, v65
	v_mul_f32_e32 v64, v192, v56
	v_mul_f32_e32 v60, v60, v68
	v_and_b32_e32 v68, 0xffff0000, v80
	v_mul_f32_e32 v64, v64, v66
	v_mul_f32_e32 v66, v190, v56
	v_mul_f32_e32 v62, v62, v68
	v_lshlrev_b32_e32 v68, 16, v81
	v_mul_f32_e32 v66, v66, v67
	v_mul_f32_e32 v64, v64, v68
	v_and_b32_e32 v68, 0xffff0000, v81
	v_mul_f32_e32 v63, v199, v56
	v_mul_f32_e32 v66, v66, v68
	s_waitcnt vmcnt(7)
	v_lshlrev_b32_e32 v68, 16, v82
	v_mul_f32_e32 v63, v63, v69
	v_mul_f32_e32 v65, v193, v56
	v_mul_f32_e32 v68, v61, v68
	v_and_b32_e32 v61, 0xffff0000, v82
	v_mul_f32_e32 v65, v65, v70
	v_mul_f32_e32 v67, v191, v56
	v_mul_f32_e32 v63, v63, v61
	v_lshlrev_b32_e32 v61, 16, v83
	v_mul_f32_e32 v67, v67, v71
	v_mul_f32_e32 v65, v65, v61
	v_and_b32_e32 v61, 0xffff0000, v83
	v_mul_f32_e32 v67, v67, v61
	v_cvt_pk_bf16_f32 v60, v60, v62
	v_cvt_pk_bf16_f32 v61, v64, v66
	v_cvt_pk_bf16_f32 v62, v68, v63
	v_cvt_pk_bf16_f32 v63, v65, v67
	v_or_b32_e32 v64, 64, v58
	v_permlane32_swap_b32_e32 v60, v62
	v_permlane32_swap_b32_e32 v61, v63
	global_store_dwordx4 v64, v[60:63], s[4:5] offset:32
	global_load_dwordx2 v[76:77], v59, s[4:5] offset:192
	global_load_dwordx2 v[78:79], v59, s[4:5] offset:208
	global_load_dwordx2 v[80:81], v59, s[4:5] offset:224
	global_load_dwordx2 v[82:83], v59, s[4:5] offset:240
	ds_read_b128 v[60:63], v57 offset:256
	ds_read_b128 v[64:67], v57 offset:288
	v_mul_f32_e32 v68, v188, v56
	v_mul_f32_e32 v44, v44, v56
	v_mul_f32_e32 v42, v42, v56
	s_waitcnt lgkmcnt(1)
	v_mul_f32_e32 v60, v68, v60
	v_mul_f32_e32 v68, v189, v56
	s_waitcnt lgkmcnt(0)
	v_mul_f32_e32 v64, v68, v64
	v_mul_f32_e32 v68, v186, v56
	v_mul_f32_e32 v61, v68, v61
	v_mul_f32_e32 v68, v187, v56
	v_mul_f32_e32 v65, v68, v65
	v_mul_f32_e32 v68, v184, v56
	v_mul_f32_e32 v62, v68, v62
	v_mul_f32_e32 v68, v185, v56
	v_mul_f32_e32 v66, v68, v66
	v_mul_f32_e32 v68, v182, v56
	v_mul_f32_e32 v63, v68, v63
	v_mul_f32_e32 v68, v183, v56
	v_mul_f32_e32 v67, v68, v67
	s_waitcnt vmcnt(9)
	v_lshlrev_b32_e32 v68, 16, v72
	v_mul_f32_e32 v60, v60, v68
	v_and_b32_e32 v68, 0xffff0000, v72
	v_mul_f32_e32 v61, v61, v68
	v_lshlrev_b32_e32 v68, 16, v73
	v_mul_f32_e32 v62, v62, v68
	v_and_b32_e32 v68, 0xffff0000, v73
	v_mul_f32_e32 v63, v63, v68
	s_waitcnt vmcnt(8)
	v_lshlrev_b32_e32 v68, 16, v74
	v_mul_f32_e32 v64, v64, v68
	v_and_b32_e32 v68, 0xffff0000, v74
	v_mul_f32_e32 v65, v65, v68
	v_lshlrev_b32_e32 v68, 16, v75
	v_mul_f32_e32 v66, v66, v68
	v_and_b32_e32 v68, 0xffff0000, v75
	v_mul_f32_e32 v67, v67, v68
	v_cvt_pk_bf16_f32 v60, v60, v61
	v_cvt_pk_bf16_f32 v61, v62, v63
	v_cvt_pk_bf16_f32 v62, v64, v65
	v_cvt_pk_bf16_f32 v63, v66, v67
	ds_read_b128 v[64:67], v57 offset:320
	ds_read_b128 v[68:71], v57 offset:352
	v_permlane32_swap_b32_e32 v60, v62
	v_permlane32_swap_b32_e32 v61, v63
	global_store_dwordx4 v58, v[60:63], s[4:5] offset:128
	v_mul_f32_e32 v40, v40, v56
	v_mul_f32_e32 v47, v47, v56
	v_mul_f32_e32 v60, v180, v56
	v_mul_f32_e32 v61, v181, v56
	s_waitcnt lgkmcnt(1)
	v_mul_f32_e32 v60, v60, v64
	s_waitcnt lgkmcnt(0)
	v_mul_f32_e32 v61, v61, v68
	v_mul_f32_e32 v62, v178, v56
	s_waitcnt vmcnt(8)
	v_lshlrev_b32_e32 v68, 16, v84
	v_mul_f32_e32 v62, v62, v65
	v_mul_f32_e32 v64, v173, v56
	v_mul_f32_e32 v60, v60, v68
	v_and_b32_e32 v68, 0xffff0000, v84
	v_mul_f32_e32 v64, v64, v66
	v_mul_f32_e32 v66, v171, v56
	v_mul_f32_e32 v62, v62, v68
	v_lshlrev_b32_e32 v68, 16, v85
	v_mul_f32_e32 v66, v66, v67
	v_mul_f32_e32 v64, v64, v68
	v_and_b32_e32 v68, 0xffff0000, v85
	v_mul_f32_e32 v63, v179, v56
	v_mul_f32_e32 v66, v66, v68
	s_waitcnt vmcnt(7)
	v_lshlrev_b32_e32 v68, 16, v86
	v_mul_f32_e32 v63, v63, v69
	v_mul_f32_e32 v65, v177, v56
	v_mul_f32_e32 v68, v61, v68
	v_and_b32_e32 v61, 0xffff0000, v86
	v_mul_f32_e32 v65, v65, v70
	v_mul_f32_e32 v67, v172, v56
	v_mul_f32_e32 v63, v63, v61
	v_lshlrev_b32_e32 v61, 16, v87
	v_mul_f32_e32 v67, v67, v71
	v_mul_f32_e32 v65, v65, v61
	v_and_b32_e32 v61, 0xffff0000, v87
	v_mul_f32_e32 v67, v67, v61
	v_cvt_pk_bf16_f32 v60, v60, v62
	v_cvt_pk_bf16_f32 v61, v64, v66
	v_cvt_pk_bf16_f32 v62, v68, v63
	v_cvt_pk_bf16_f32 v63, v65, v67
	v_or_b32_e32 v64, 0x80, v58
	v_permlane32_swap_b32_e32 v60, v62
	v_permlane32_swap_b32_e32 v61, v63
	global_store_dwordx4 v64, v[60:63], s[4:5] offset:32
	global_load_dwordx2 v[72:73], v59, s[4:5] offset:256
	global_load_dwordx2 v[74:75], v59, s[4:5] offset:272
	global_load_dwordx2 v[84:85], v59, s[4:5] offset:288
	global_load_dwordx2 v[86:87], v59, s[4:5] offset:304
	ds_read_b128 v[60:63], v57 offset:384
	ds_read_b128 v[64:67], v57 offset:416
	v_mul_f32_e32 v68, v163, v56
	v_mul_f32_e32 v45, v45, v56
	v_mul_f32_e32 v43, v43, v56
	s_waitcnt lgkmcnt(1)
	v_mul_f32_e32 v60, v68, v60
	v_mul_f32_e32 v68, v170, v56
	s_waitcnt lgkmcnt(0)
	v_mul_f32_e32 v64, v68, v64
	v_mul_f32_e32 v68, v160, v56
	v_mul_f32_e32 v61, v68, v61
	v_mul_f32_e32 v68, v162, v56
	v_mul_f32_e32 v65, v68, v65
	v_mul_f32_e32 v68, v158, v56
	v_mul_f32_e32 v62, v68, v62
	v_mul_f32_e32 v68, v159, v56
	v_mul_f32_e32 v66, v68, v66
	v_mul_f32_e32 v68, v156, v56
	v_mul_f32_e32 v63, v68, v63
	v_mul_f32_e32 v68, v157, v56
	v_mul_f32_e32 v67, v68, v67
	s_waitcnt vmcnt(9)
	v_lshlrev_b32_e32 v68, 16, v76
	v_mul_f32_e32 v60, v60, v68
	v_and_b32_e32 v68, 0xffff0000, v76
	v_mul_f32_e32 v61, v61, v68
	v_lshlrev_b32_e32 v68, 16, v77
	v_mul_f32_e32 v62, v62, v68
	v_and_b32_e32 v68, 0xffff0000, v77
	v_mul_f32_e32 v63, v63, v68
	s_waitcnt vmcnt(8)
	v_lshlrev_b32_e32 v68, 16, v78
	v_mul_f32_e32 v64, v64, v68
	v_and_b32_e32 v68, 0xffff0000, v78
	v_mul_f32_e32 v65, v65, v68
	v_lshlrev_b32_e32 v68, 16, v79
	v_mul_f32_e32 v66, v66, v68
	v_and_b32_e32 v68, 0xffff0000, v79
	v_mul_f32_e32 v67, v67, v68
	v_cvt_pk_bf16_f32 v60, v60, v61
	v_cvt_pk_bf16_f32 v61, v62, v63
	v_cvt_pk_bf16_f32 v62, v64, v65
	v_cvt_pk_bf16_f32 v63, v66, v67
	ds_read_b128 v[64:67], v57 offset:448
	ds_read_b128 v[68:71], v57 offset:480
	v_permlane32_swap_b32_e32 v60, v62
	v_permlane32_swap_b32_e32 v61, v63
	global_store_dwordx4 v58, v[60:63], s[4:5] offset:192
	v_mul_f32_e32 v41, v41, v56
	v_mul_f32_e32 v38, v38, v56
	v_mul_f32_e32 v60, v126, v56
	v_mul_f32_e32 v61, v127, v56
	s_waitcnt lgkmcnt(1)
	v_mul_f32_e32 v60, v60, v64
	s_waitcnt lgkmcnt(0)
	v_mul_f32_e32 v61, v61, v68
	v_mul_f32_e32 v62, v124, v56
	s_waitcnt vmcnt(8)
	v_lshlrev_b32_e32 v68, 16, v80
	v_mul_f32_e32 v62, v62, v65
	v_mul_f32_e32 v64, v122, v56
	v_mul_f32_e32 v60, v60, v68
	v_and_b32_e32 v68, 0xffff0000, v80
	v_mul_f32_e32 v64, v64, v66
	v_mul_f32_e32 v66, v120, v56
	v_mul_f32_e32 v62, v62, v68
	v_lshlrev_b32_e32 v68, 16, v81
	v_mul_f32_e32 v66, v66, v67
	v_mul_f32_e32 v64, v64, v68
	v_and_b32_e32 v68, 0xffff0000, v81
	v_mul_f32_e32 v63, v125, v56
	v_mul_f32_e32 v66, v66, v68
	s_waitcnt vmcnt(7)
	v_lshlrev_b32_e32 v68, 16, v82
	v_mul_f32_e32 v63, v63, v69
	v_mul_f32_e32 v65, v123, v56
	v_mul_f32_e32 v68, v61, v68
	v_and_b32_e32 v61, 0xffff0000, v82
	v_mul_f32_e32 v65, v65, v70
	v_mul_f32_e32 v67, v121, v56
	v_mul_f32_e32 v63, v63, v61
	v_lshlrev_b32_e32 v61, 16, v83
	v_mul_f32_e32 v67, v67, v71
	v_mul_f32_e32 v65, v65, v61
	v_and_b32_e32 v61, 0xffff0000, v83
	v_mul_f32_e32 v67, v67, v61
	v_cvt_pk_bf16_f32 v60, v60, v62
	v_cvt_pk_bf16_f32 v61, v64, v66
	v_cvt_pk_bf16_f32 v62, v68, v63
	v_cvt_pk_bf16_f32 v63, v65, v67
	v_or_b32_e32 v64, 0xc0, v58
	v_permlane32_swap_b32_e32 v60, v62
	v_permlane32_swap_b32_e32 v61, v63
	global_store_dwordx4 v64, v[60:63], s[4:5] offset:32
	global_load_dwordx2 v[76:77], v59, s[4:5] offset:320
	global_load_dwordx2 v[78:79], v59, s[4:5] offset:336
	global_load_dwordx2 v[80:81], v59, s[4:5] offset:352
	global_load_dwordx2 v[82:83], v59, s[4:5] offset:368
	ds_read_b128 v[60:63], v57 offset:512
	ds_read_b128 v[64:67], v57 offset:544
	v_mul_f32_e32 v68, v118, v56
	v_mul_f32_e32 v36, v36, v56
	v_mul_f32_e32 v34, v34, v56
	s_waitcnt lgkmcnt(1)
	v_mul_f32_e32 v60, v68, v60
	v_mul_f32_e32 v68, v119, v56
	s_waitcnt lgkmcnt(0)
	v_mul_f32_e32 v64, v68, v64
	v_mul_f32_e32 v68, v116, v56
	v_mul_f32_e32 v61, v68, v61
	v_mul_f32_e32 v68, v117, v56
	v_mul_f32_e32 v65, v68, v65
	v_mul_f32_e32 v68, v114, v56
	v_mul_f32_e32 v62, v68, v62
	v_mul_f32_e32 v68, v115, v56
	v_mul_f32_e32 v66, v68, v66
	v_mul_f32_e32 v68, v112, v56
	v_mul_f32_e32 v63, v68, v63
	v_mul_f32_e32 v68, v113, v56
	v_mul_f32_e32 v67, v68, v67
	s_waitcnt vmcnt(9)
	v_lshlrev_b32_e32 v68, 16, v72
	v_mul_f32_e32 v60, v60, v68
	v_and_b32_e32 v68, 0xffff0000, v72
	v_mul_f32_e32 v61, v61, v68
	v_lshlrev_b32_e32 v68, 16, v73
	v_mul_f32_e32 v62, v62, v68
	v_and_b32_e32 v68, 0xffff0000, v73
	v_mul_f32_e32 v63, v63, v68
	s_waitcnt vmcnt(8)
	v_lshlrev_b32_e32 v68, 16, v74
	v_mul_f32_e32 v64, v64, v68
	v_and_b32_e32 v68, 0xffff0000, v74
	v_mul_f32_e32 v65, v65, v68
	v_lshlrev_b32_e32 v68, 16, v75
	v_mul_f32_e32 v66, v66, v68
	v_and_b32_e32 v68, 0xffff0000, v75
	v_mul_f32_e32 v67, v67, v68
	v_cvt_pk_bf16_f32 v60, v60, v61
	v_cvt_pk_bf16_f32 v61, v62, v63
	v_cvt_pk_bf16_f32 v62, v64, v65
	v_cvt_pk_bf16_f32 v63, v66, v67
	ds_read_b128 v[64:67], v57 offset:576
	ds_read_b128 v[68:71], v57 offset:608
	v_permlane32_swap_b32_e32 v60, v62
	v_permlane32_swap_b32_e32 v61, v63
	global_store_dwordx4 v58, v[60:63], s[4:5] offset:256
	s_waitcnt lgkmcnt(1)
	v_mul_f32_e32 v54, v54, v64
	v_mul_f32_e32 v52, v52, v65
	s_waitcnt vmcnt(8)
	v_lshlrev_b32_e32 v60, 16, v84
	v_mul_f32_e32 v54, v54, v60
	v_and_b32_e32 v60, 0xffff0000, v84
	v_mul_f32_e32 v50, v50, v66
	v_mul_f32_e32 v52, v52, v60
	v_lshlrev_b32_e32 v60, 16, v85
	v_mul_f32_e32 v48, v48, v67
	v_mul_f32_e32 v50, v50, v60
	v_and_b32_e32 v60, 0xffff0000, v85
	s_waitcnt lgkmcnt(0)
	v_mul_f32_e32 v55, v55, v68
	v_mul_f32_e32 v60, v48, v60
	s_waitcnt vmcnt(7)
	v_lshlrev_b32_e32 v48, 16, v86
	v_mul_f32_e32 v53, v53, v69
	v_mul_f32_e32 v55, v55, v48
	v_and_b32_e32 v48, 0xffff0000, v86
	v_mul_f32_e32 v51, v51, v70
	v_mul_f32_e32 v53, v53, v48
	v_lshlrev_b32_e32 v48, 16, v87
	v_mul_f32_e32 v49, v49, v71
	v_mul_f32_e32 v51, v51, v48
	v_and_b32_e32 v48, 0xffff0000, v87
	v_mul_f32_e32 v61, v49, v48
	v_cvt_pk_bf16_f32 v48, v54, v52
	v_cvt_pk_bf16_f32 v49, v50, v60
	v_cvt_pk_bf16_f32 v50, v55, v53
	v_cvt_pk_bf16_f32 v51, v51, v61
	v_or_b32_e32 v52, 0x100, v58
	v_permlane32_swap_b32_e32 v48, v50
	v_permlane32_swap_b32_e32 v49, v51
	global_store_dwordx4 v52, v[48:51], s[4:5] offset:32
	global_load_dwordx2 v[60:61], v59, s[4:5] offset:384
	global_load_dwordx2 v[62:63], v59, s[4:5] offset:400
	global_load_dwordx2 v[64:65], v59, s[4:5] offset:416
	global_load_dwordx2 v[66:67], v59, s[4:5] offset:432
	ds_read_b128 v[48:51], v57 offset:640
	ds_read_b128 v[52:55], v57 offset:672
	v_mul_f32_e32 v32, v32, v56
	v_mul_f32_e32 v39, v39, v56
	v_mul_f32_e32 v37, v37, v56
	s_waitcnt lgkmcnt(1)
	v_mul_f32_e32 v46, v46, v48
	s_waitcnt vmcnt(9)
	v_lshlrev_b32_e32 v48, 16, v76
	v_mul_f32_e32 v44, v44, v49
	v_mul_f32_e32 v46, v46, v48
	v_and_b32_e32 v48, 0xffff0000, v76
	v_mul_f32_e32 v42, v42, v50
	v_mul_f32_e32 v44, v44, v48
	v_lshlrev_b32_e32 v48, 16, v77
	v_mul_f32_e32 v40, v40, v51
	v_mul_f32_e32 v42, v42, v48
	v_and_b32_e32 v48, 0xffff0000, v77
	s_waitcnt lgkmcnt(0)
	v_mul_f32_e32 v47, v47, v52
	v_mul_f32_e32 v48, v40, v48
	s_waitcnt vmcnt(8)
	v_lshlrev_b32_e32 v40, 16, v78
	v_mul_f32_e32 v45, v45, v53
	v_mul_f32_e32 v47, v47, v40
	v_and_b32_e32 v40, 0xffff0000, v78
	v_mul_f32_e32 v43, v43, v54
	v_mul_f32_e32 v45, v45, v40
	v_lshlrev_b32_e32 v40, 16, v79
	v_mul_f32_e32 v41, v41, v55
	v_mul_f32_e32 v43, v43, v40
	v_and_b32_e32 v40, 0xffff0000, v79
	v_mul_f32_e32 v49, v41, v40
	v_cvt_pk_bf16_f32 v40, v46, v44
	v_cvt_pk_bf16_f32 v41, v42, v48
	v_cvt_pk_bf16_f32 v42, v47, v45
	v_cvt_pk_bf16_f32 v43, v43, v49
	ds_read_b128 v[44:47], v57 offset:704
	ds_read_b128 v[48:51], v57 offset:736
	v_permlane32_swap_b32_e32 v40, v42
	v_permlane32_swap_b32_e32 v41, v43
	global_store_dwordx4 v58, v[40:43], s[4:5] offset:320
	s_waitcnt lgkmcnt(1)
	v_mul_f32_e32 v38, v38, v44
	v_mul_f32_e32 v36, v36, v45
	s_waitcnt vmcnt(8)
	v_lshlrev_b32_e32 v40, 16, v80
	v_mul_f32_e32 v38, v38, v40
	v_and_b32_e32 v40, 0xffff0000, v80
	v_mul_f32_e32 v34, v34, v46
	v_mul_f32_e32 v36, v36, v40
	v_lshlrev_b32_e32 v40, 16, v81
	v_mul_f32_e32 v32, v32, v47
	v_mul_f32_e32 v34, v34, v40
	v_and_b32_e32 v40, 0xffff0000, v81
	s_waitcnt lgkmcnt(0)
	v_mul_f32_e32 v39, v39, v48
	v_mul_f32_e32 v40, v32, v40
	s_waitcnt vmcnt(7)
	v_lshlrev_b32_e32 v32, 16, v82
	v_mul_f32_e32 v37, v37, v49
	v_mul_f32_e32 v35, v35, v56
	v_mul_f32_e32 v39, v39, v32
	v_and_b32_e32 v32, 0xffff0000, v82
	v_mul_f32_e32 v35, v35, v50
	v_mul_f32_e32 v33, v33, v56
	v_mul_f32_e32 v37, v37, v32
	v_lshlrev_b32_e32 v32, 16, v83
	v_mul_f32_e32 v33, v33, v51
	v_mul_f32_e32 v35, v35, v32
	v_and_b32_e32 v32, 0xffff0000, v83
	v_mul_f32_e32 v41, v33, v32
	v_cvt_pk_bf16_f32 v32, v38, v36
	v_cvt_pk_bf16_f32 v33, v34, v40
	v_cvt_pk_bf16_f32 v34, v39, v37
	v_cvt_pk_bf16_f32 v35, v35, v41
	v_or_b32_e32 v36, 0x140, v58
	v_permlane32_swap_b32_e32 v32, v34
	v_permlane32_swap_b32_e32 v33, v35
	global_store_dwordx4 v36, v[32:35], s[4:5] offset:32
	global_load_dwordx2 v[40:41], v59, s[4:5] offset:448
	global_load_dwordx2 v[42:43], v59, s[4:5] offset:464
	global_load_dwordx2 v[44:45], v59, s[4:5] offset:480
	global_load_dwordx2 v[46:47], v59, s[4:5] offset:496
	ds_read_b128 v[32:35], v57 offset:768
	ds_read_b128 v[36:39], v57 offset:800
	v_mul_f32_e32 v30, v30, v56
	v_mul_f32_e32 v28, v28, v56
	v_mul_f32_e32 v26, v26, v56
	s_waitcnt lgkmcnt(1)
	v_mul_f32_e32 v30, v30, v32
	s_waitcnt vmcnt(9)
	v_lshlrev_b32_e32 v32, 16, v60
	v_mul_f32_e32 v28, v28, v33
	v_mul_f32_e32 v30, v30, v32
	v_and_b32_e32 v32, 0xffff0000, v60
	v_mul_f32_e32 v26, v26, v34
	v_mul_f32_e32 v24, v24, v56
	v_mul_f32_e32 v28, v28, v32
	v_lshlrev_b32_e32 v32, 16, v61
	v_mul_f32_e32 v31, v31, v56
	v_mul_f32_e32 v24, v24, v35
	v_mul_f32_e32 v26, v26, v32
	v_and_b32_e32 v32, 0xffff0000, v61
	s_waitcnt lgkmcnt(0)
	v_mul_f32_e32 v31, v31, v36
	v_mul_f32_e32 v29, v29, v56
	v_mul_f32_e32 v32, v24, v32
	s_waitcnt vmcnt(8)
	v_lshlrev_b32_e32 v24, 16, v62
	v_mul_f32_e32 v29, v29, v37
	v_mul_f32_e32 v27, v27, v56
	v_mul_f32_e32 v31, v31, v24
	v_and_b32_e32 v24, 0xffff0000, v62
	v_mul_f32_e32 v27, v27, v38
	v_mul_f32_e32 v25, v25, v56
	v_mul_f32_e32 v29, v29, v24
	v_lshlrev_b32_e32 v24, 16, v63
	v_mul_f32_e32 v25, v25, v39
	v_mul_f32_e32 v27, v27, v24
	v_and_b32_e32 v24, 0xffff0000, v63
	v_mul_f32_e32 v33, v25, v24
	v_cvt_pk_bf16_f32 v24, v30, v28
	v_cvt_pk_bf16_f32 v25, v26, v32
	v_cvt_pk_bf16_f32 v26, v31, v29
	v_cvt_pk_bf16_f32 v27, v27, v33
	ds_read_b128 v[28:31], v57 offset:832
	ds_read_b128 v[32:35], v57 offset:864
	v_permlane32_swap_b32_e32 v24, v26
	v_permlane32_swap_b32_e32 v25, v27
	v_mul_f32_e32 v22, v22, v56
	global_store_dwordx4 v58, v[24:27], s[4:5] offset:384
	s_waitcnt lgkmcnt(1)
	v_mul_f32_e32 v22, v22, v28
	v_mul_f32_e32 v20, v20, v56
	s_waitcnt vmcnt(8)
	v_lshlrev_b32_e32 v24, 16, v64
	v_mul_f32_e32 v20, v20, v29
	v_mul_f32_e32 v18, v18, v56
	v_mul_f32_e32 v22, v22, v24
	v_and_b32_e32 v24, 0xffff0000, v64
	v_mul_f32_e32 v18, v18, v30
	v_mul_f32_e32 v16, v16, v56
	v_mul_f32_e32 v20, v20, v24
	v_lshlrev_b32_e32 v24, 16, v65
	v_mul_f32_e32 v23, v23, v56
	v_mul_f32_e32 v16, v16, v31
	v_mul_f32_e32 v18, v18, v24
	v_and_b32_e32 v24, 0xffff0000, v65
	s_waitcnt lgkmcnt(0)
	v_mul_f32_e32 v23, v23, v32
	v_mul_f32_e32 v21, v21, v56
	v_mul_f32_e32 v24, v16, v24
	s_waitcnt vmcnt(7)
	v_lshlrev_b32_e32 v16, 16, v66
	v_mul_f32_e32 v21, v21, v33
	v_mul_f32_e32 v19, v19, v56
	v_mul_f32_e32 v23, v23, v16
	v_and_b32_e32 v16, 0xffff0000, v66
	v_mul_f32_e32 v19, v19, v34
	v_mul_f32_e32 v17, v17, v56
	v_mul_f32_e32 v21, v21, v16
	v_lshlrev_b32_e32 v16, 16, v67
	v_mul_f32_e32 v17, v17, v35
	v_mul_f32_e32 v19, v19, v16
	v_and_b32_e32 v16, 0xffff0000, v67
	v_mul_f32_e32 v25, v17, v16
	v_cvt_pk_bf16_f32 v16, v22, v20
	v_cvt_pk_bf16_f32 v17, v18, v24
	v_cvt_pk_bf16_f32 v18, v23, v21
	v_cvt_pk_bf16_f32 v19, v19, v25
	v_or_b32_e32 v20, 0x180, v58
	v_permlane32_swap_b32_e32 v16, v18
	v_permlane32_swap_b32_e32 v17, v19
	global_store_dwordx4 v20, v[16:19], s[4:5] offset:32
	ds_read_b128 v[16:19], v57 offset:896
	ds_read_b128 v[20:23], v57 offset:928
	v_mul_f32_e32 v14, v14, v56
	v_mul_f32_e32 v12, v12, v56
	v_mul_f32_e32 v10, v10, v56
	s_waitcnt lgkmcnt(1)
	v_mul_f32_e32 v14, v14, v16
	s_waitcnt vmcnt(5)
	v_lshlrev_b32_e32 v16, 16, v40
	v_mul_f32_e32 v12, v12, v17
	v_mul_f32_e32 v14, v14, v16
	v_and_b32_e32 v16, 0xffff0000, v40
	v_mul_f32_e32 v10, v10, v18
	v_mul_f32_e32 v8, v8, v56
	v_mul_f32_e32 v12, v12, v16
	v_lshlrev_b32_e32 v16, 16, v41
	v_mul_f32_e32 v15, v15, v56
	v_mul_f32_e32 v8, v8, v19
	v_mul_f32_e32 v10, v10, v16
	v_and_b32_e32 v16, 0xffff0000, v41
	s_waitcnt lgkmcnt(0)
	v_mul_f32_e32 v15, v15, v20
	v_mul_f32_e32 v13, v13, v56
	v_mul_f32_e32 v16, v8, v16
	s_waitcnt vmcnt(4)
	v_lshlrev_b32_e32 v8, 16, v42
	v_mul_f32_e32 v13, v13, v21
	v_mul_f32_e32 v11, v11, v56
	v_mul_f32_e32 v15, v15, v8
	v_and_b32_e32 v8, 0xffff0000, v42
	v_mul_f32_e32 v11, v11, v22
	v_mul_f32_e32 v9, v9, v56
	v_mul_f32_e32 v13, v13, v8
	v_lshlrev_b32_e32 v8, 16, v43
	v_mul_f32_e32 v9, v9, v23
	v_mul_f32_e32 v11, v11, v8
	v_and_b32_e32 v8, 0xffff0000, v43
	v_mul_f32_e32 v17, v9, v8
	v_cvt_pk_bf16_f32 v8, v14, v12
	v_cvt_pk_bf16_f32 v9, v10, v16
	v_cvt_pk_bf16_f32 v10, v15, v13
	v_cvt_pk_bf16_f32 v11, v11, v17
	ds_read_b128 v[12:15], v57 offset:960
	ds_read_b128 v[16:19], v57 offset:992
	v_permlane32_swap_b32_e32 v8, v10
	v_permlane32_swap_b32_e32 v9, v11
	v_mul_f32_e32 v6, v6, v56
	global_store_dwordx4 v58, v[8:11], s[4:5] offset:448
	s_waitcnt lgkmcnt(1)
	v_mul_f32_e32 v6, v6, v12
	v_mul_f32_e32 v4, v4, v56
	s_waitcnt vmcnt(4)
	v_lshlrev_b32_e32 v8, 16, v44
	v_mul_f32_e32 v4, v4, v13
	v_mul_f32_e32 v2, v2, v56
	v_mul_f32_e32 v6, v6, v8
	v_and_b32_e32 v8, 0xffff0000, v44
	v_mul_f32_e32 v2, v2, v14
	v_mul_f32_e32 v0, v0, v56
	v_mul_f32_e32 v4, v4, v8
	v_lshlrev_b32_e32 v8, 16, v45
	v_mul_f32_e32 v7, v7, v56
	v_mul_f32_e32 v0, v0, v15
	v_mul_f32_e32 v2, v2, v8
	v_and_b32_e32 v8, 0xffff0000, v45
	s_waitcnt lgkmcnt(0)
	v_mul_f32_e32 v7, v7, v16
	v_mul_f32_e32 v5, v5, v56
	v_mul_f32_e32 v8, v0, v8
	s_waitcnt vmcnt(3)
	v_lshlrev_b32_e32 v0, 16, v46
	v_mul_f32_e32 v5, v5, v17
	v_mul_f32_e32 v3, v3, v56
	v_mul_f32_e32 v7, v7, v0
	v_and_b32_e32 v0, 0xffff0000, v46
	v_mul_f32_e32 v3, v3, v18
	v_mul_f32_e32 v1, v1, v56
	v_mul_f32_e32 v5, v5, v0
	v_lshlrev_b32_e32 v0, 16, v47
	v_mul_f32_e32 v1, v1, v19
	v_mul_f32_e32 v3, v3, v0
	v_and_b32_e32 v0, 0xffff0000, v47
	v_mul_f32_e32 v9, v1, v0
	v_cvt_pk_bf16_f32 v0, v6, v4
	v_cvt_pk_bf16_f32 v1, v2, v8
	v_cvt_pk_bf16_f32 v2, v7, v5
	v_cvt_pk_bf16_f32 v3, v3, v9
	v_readlane_b32 s2, v255, 38
	v_permlane32_swap_b32_e32 v0, v2
	v_permlane32_swap_b32_e32 v1, v3
	v_or_b32_e32 v4, 0x1c0, v58
	s_cmp_lg_u32 s10, s2
	s_mov_b32 s2, s10
	global_store_dwordx4 v4, v[0:3], s[4:5] offset:32
	s_cbranch_scc0 .LBB0_541

.Lstg_b6:
	s_add_i32 s6, s88, -1
	s_cmp_ge_u32 s6, s89
	s_cselect_b64 s[82:83], -1, 0
	s_mov_b64 s[4:5], -1
	s_and_b64 vcc, exec, s[82:83]
	s_cbranch_vccz .LBB0_524
	v_mov_b32_e32 v144, s0
	ds_read_b32 v146, v144
	ds_read_b32 v144, v144 offset:4
	s_waitcnt vmcnt(0) lgkmcnt(0)
	v_readfirstlane_b32 s4, v146
	v_readfirstlane_b32 s5, v144
	s_nop 1
	s_nop 3
	s_mov_b32 m0, s2
	s_nop 0
	global_load_lds_dwordx4 v170, s[4:5]
	s_nop 3
	s_mov_b32 m0, s91
	s_nop 0
	global_load_lds_dwordx4 v172, s[4:5]
	s_mov_b64 s[4:5], 0

.Lstg_b7:
	s_cmp_gt_u32 s88, s89
	s_cbranch_scc1 .LBB0_533
	s_cmp_ge_u32 s88, s89
	s_mov_b64 s[4:5], -1
	s_cbranch_scc0 .LBB0_531
	v_mov_b32_e32 v194, s0
	ds_read_b32 v196, v194
	ds_read_b32 v194, v194 offset:4
	s_waitcnt vmcnt(0) lgkmcnt(0)
	v_readfirstlane_b32 s4, v196
	v_readfirstlane_b32 s5, v194
	s_nop 1
	s_nop 3
	s_mov_b32 m0, s2
	s_nop 0
	global_load_lds_dwordx4 v170, s[4:5]
	s_nop 3
	s_mov_b32 m0, s91
	s_nop 0
	global_load_lds_dwordx4 v172, s[4:5]
	s_mov_b64 s[4:5], 0

.LBB0_533:
	s_mov_b64 s[4:5], -1
	s_and_b64 vcc, exec, s[82:83]
	s_cbranch_vccz .LBB0_535
	v_mov_b32_e32 v194, s70
	ds_read_b32 v196, v194
	ds_read_b32 v194, v194 offset:4
	s_waitcnt vmcnt(0) lgkmcnt(0)
	v_readfirstlane_b32 s4, v196
	v_readfirstlane_b32 s5, v194
	s_nop 1
	s_nop 3
	s_mov_b32 m0, s81
	s_nop 0
	global_load_lds_dwordx4 v162, s[4:5]
	s_nop 3
	s_add_i32 m0, s78, 0xffffff80
	s_nop 0
	global_load_lds_dwordx4 v162, s[4:5] offset:128
	s_add_i32 m0, s69, 0xffffff00
	s_nop 0
	global_load_lds_dwordx4 v162, s[4:5] offset:256
	s_add_i32 m0, s68, 0xfffffe80
	s_nop 0
	global_load_lds_dwordx4 v162, s[4:5] offset:384
	s_mov_b64 s[4:5], 0

.Lstg_b14:
	s_add_i32 s8, s3, -1
	s_cmp_ge_u32 s8, s75
	s_cselect_b64 s[96:97], -1, 0
	s_mov_b64 s[6:7], -1
	s_and_b64 vcc, exec, s[96:97]
	s_cbranch_vccz .LBB0_561
	v_mov_b32_e32 v144, s80
	ds_read_b32 v146, v144
	ds_read_b32 v144, v144 offset:4
	s_waitcnt vmcnt(0) lgkmcnt(0)
	v_readfirstlane_b32 s6, v146
	v_readfirstlane_b32 s7, v144
	s_nop 1
	s_nop 3
	s_mov_b32 m0, s83
	s_nop 0
	global_load_lds_dwordx4 v160, s[6:7]
	s_nop 3
	s_mov_b32 m0, s78
	s_nop 0
	global_load_lds_dwordx4 v170, s[6:7]
	s_mov_b64 s[6:7], 0

.Lstg_b15:
	s_cmp_gt_u32 s3, s75
	s_cbranch_scc1 .LBB0_572
	s_cmp_ge_u32 s3, s75
	s_mov_b64 s[6:7], -1
	s_cbranch_scc0 .LBB0_570
	v_mov_b32_e32 v148, s80
	ds_read_b32 v144, v148
	ds_read_b32 v147, v148 offset:4
	s_waitcnt vmcnt(0) lgkmcnt(0)
	v_readfirstlane_b32 s6, v144
	v_readfirstlane_b32 s7, v147
	s_nop 1
	s_nop 3
	s_mov_b32 m0, s83
	s_nop 0
	global_load_lds_dwordx4 v160, s[6:7]
	s_nop 3
	s_mov_b32 m0, s78
	s_nop 0
	global_load_lds_dwordx4 v170, s[6:7]
	s_mov_b64 s[6:7], 0

.LBB0_572:
	s_mov_b64 s[6:7], -1
	s_and_b64 vcc, exec, s[96:97]
	s_cbranch_vccz .LBB0_574
	v_mov_b32_e32 v148, s0
	ds_read_b32 v144, v148
	ds_read_b32 v147, v148 offset:4
	s_waitcnt vmcnt(0) lgkmcnt(0)
	v_readfirstlane_b32 s6, v144
	v_readfirstlane_b32 s7, v147
	s_nop 1
	s_nop 3
	s_mov_b32 m0, s93
	s_nop 0
	global_load_lds_dwordx4 v162, s[6:7]
	s_nop 3
	s_add_i32 m0, s2, 0xffffff80
	s_nop 0
	global_load_lds_dwordx4 v162, s[6:7] offset:128
	s_add_i32 m0, s69, 0xffffff00
	s_nop 0
	global_load_lds_dwordx4 v162, s[6:7] offset:256
	s_add_i32 m0, s68, 0xfffffe80
	s_nop 0
	global_load_lds_dwordx4 v162, s[6:7] offset:384
	s_mov_b64 s[6:7], 0

.Lstg_b16:
	v_mov_b32_e32 v146, s0
	ds_read_b32 v148, v146
	ds_read_b32 v146, v146 offset:4
	s_waitcnt vmcnt(0) lgkmcnt(0)
	v_readfirstlane_b32 s4, v148
	v_readfirstlane_b32 s5, v146
	s_nop 1
	s_nop 3
	s_mov_b32 m0, s93
	s_nop 0
	global_load_lds_dwordx4 v162, s[4:5]
	s_nop 3
	s_add_i32 m0, s2, 0xffffff80
	s_nop 0
	global_load_lds_dwordx4 v162, s[4:5] offset:128
	s_add_i32 m0, s69, 0xffffff00
	s_nop 0
	global_load_lds_dwordx4 v162, s[4:5] offset:256
	s_add_i32 m0, s68, 0xfffffe80
	s_nop 0
	global_load_lds_dwordx4 v162, s[4:5] offset:384
	v_cmp_gt_f32_e32 vcc, 1.0, v160
	s_cbranch_vccz .LBB0_584
	v_pk_mul_f32 v[126:127], v[126:127], v[160:161] op_sel_hi:[1,0]
	v_pk_mul_f32 v[124:125], v[124:125], v[160:161] op_sel_hi:[1,0]
	v_pk_mul_f32 v[122:123], v[122:123], v[160:161] op_sel_hi:[1,0]
	v_pk_mul_f32 v[120:121], v[120:121], v[160:161] op_sel_hi:[1,0]
	v_pk_mul_f32 v[118:119], v[118:119], v[160:161] op_sel_hi:[1,0]
	v_pk_mul_f32 v[116:117], v[116:117], v[160:161] op_sel_hi:[1,0]
	v_pk_mul_f32 v[114:115], v[114:115], v[160:161] op_sel_hi:[1,0]
	v_pk_mul_f32 v[112:113], v[112:113], v[160:161] op_sel_hi:[1,0]
	v_pk_mul_f32 v[94:95], v[94:95], v[160:161] op_sel_hi:[1,0]
	v_pk_mul_f32 v[92:93], v[92:93], v[160:161] op_sel_hi:[1,0]
	v_pk_mul_f32 v[90:91], v[90:91], v[160:161] op_sel_hi:[1,0]
	v_pk_mul_f32 v[88:89], v[88:89], v[160:161] op_sel_hi:[1,0]
	v_pk_mul_f32 v[86:87], v[86:87], v[160:161] op_sel_hi:[1,0]
	v_pk_mul_f32 v[84:85], v[84:85], v[160:161] op_sel_hi:[1,0]
	v_pk_mul_f32 v[82:83], v[82:83], v[160:161] op_sel_hi:[1,0]
	v_pk_mul_f32 v[80:81], v[80:81], v[160:161] op_sel_hi:[1,0]
	v_pk_mul_f32 v[110:111], v[110:111], v[160:161] op_sel_hi:[1,0]
	v_pk_mul_f32 v[108:109], v[108:109], v[160:161] op_sel_hi:[1,0]
	v_pk_mul_f32 v[106:107], v[106:107], v[160:161] op_sel_hi:[1,0]
	v_pk_mul_f32 v[104:105], v[104:105], v[160:161] op_sel_hi:[1,0]
	v_pk_mul_f32 v[102:103], v[102:103], v[160:161] op_sel_hi:[1,0]
	v_pk_mul_f32 v[100:101], v[100:101], v[160:161] op_sel_hi:[1,0]
	v_pk_mul_f32 v[98:99], v[98:99], v[160:161] op_sel_hi:[1,0]
	v_pk_mul_f32 v[96:97], v[96:97], v[160:161] op_sel_hi:[1,0]
	v_pk_mul_f32 v[78:79], v[78:79], v[160:161] op_sel_hi:[1,0]
	v_pk_mul_f32 v[76:77], v[76:77], v[160:161] op_sel_hi:[1,0]
	v_pk_mul_f32 v[74:75], v[74:75], v[160:161] op_sel_hi:[1,0]
	v_pk_mul_f32 v[72:73], v[72:73], v[160:161] op_sel_hi:[1,0]
	v_pk_mul_f32 v[70:71], v[70:71], v[160:161] op_sel_hi:[1,0]
	v_pk_mul_f32 v[68:69], v[68:69], v[160:161] op_sel_hi:[1,0]
	v_pk_mul_f32 v[66:67], v[66:67], v[160:161] op_sel_hi:[1,0]
	v_pk_mul_f32 v[64:65], v[64:65], v[160:161] op_sel_hi:[1,0]
	v_pk_mul_f32 v[62:63], v[62:63], v[160:161] op_sel_hi:[1,0]
	v_pk_mul_f32 v[60:61], v[60:61], v[160:161] op_sel_hi:[1,0]
	v_pk_mul_f32 v[58:59], v[58:59], v[160:161] op_sel_hi:[1,0]
	v_pk_mul_f32 v[56:57], v[56:57], v[160:161] op_sel_hi:[1,0]
	v_pk_mul_f32 v[54:55], v[54:55], v[160:161] op_sel_hi:[1,0]
	v_pk_mul_f32 v[52:53], v[52:53], v[160:161] op_sel_hi:[1,0]
	v_pk_mul_f32 v[50:51], v[50:51], v[160:161] op_sel_hi:[1,0]
	v_pk_mul_f32 v[48:49], v[48:49], v[160:161] op_sel_hi:[1,0]
	v_pk_mul_f32 v[46:47], v[46:47], v[160:161] op_sel_hi:[1,0]
	v_pk_mul_f32 v[44:45], v[44:45], v[160:161] op_sel_hi:[1,0]
	v_pk_mul_f32 v[42:43], v[42:43], v[160:161] op_sel_hi:[1,0]
	v_pk_mul_f32 v[40:41], v[40:41], v[160:161] op_sel_hi:[1,0]
	v_pk_mul_f32 v[38:39], v[38:39], v[160:161] op_sel_hi:[1,0]
	v_pk_mul_f32 v[36:37], v[36:37], v[160:161] op_sel_hi:[1,0]
	v_pk_mul_f32 v[34:35], v[34:35], v[160:161] op_sel_hi:[1,0]
	v_pk_mul_f32 v[32:33], v[32:33], v[160:161] op_sel_hi:[1,0]
	v_pk_mul_f32 v[30:31], v[30:31], v[160:161] op_sel_hi:[1,0]
	v_pk_mul_f32 v[28:29], v[28:29], v[160:161] op_sel_hi:[1,0]
	v_pk_mul_f32 v[26:27], v[26:27], v[160:161] op_sel_hi:[1,0]
	v_pk_mul_f32 v[24:25], v[24:25], v[160:161] op_sel_hi:[1,0]
	v_pk_mul_f32 v[22:23], v[22:23], v[160:161] op_sel_hi:[1,0]
	v_pk_mul_f32 v[20:21], v[20:21], v[160:161] op_sel_hi:[1,0]
	v_pk_mul_f32 v[18:19], v[18:19], v[160:161] op_sel_hi:[1,0]
	v_pk_mul_f32 v[16:17], v[16:17], v[160:161] op_sel_hi:[1,0]
	v_pk_mul_f32 v[14:15], v[14:15], v[160:161] op_sel_hi:[1,0]
	v_pk_mul_f32 v[12:13], v[12:13], v[160:161] op_sel_hi:[1,0]
	v_pk_mul_f32 v[10:11], v[10:11], v[160:161] op_sel_hi:[1,0]
	v_pk_mul_f32 v[8:9], v[8:9], v[160:161] op_sel_hi:[1,0]
	v_pk_mul_f32 v[6:7], v[6:7], v[160:161] op_sel_hi:[1,0]
	v_pk_mul_f32 v[4:5], v[4:5], v[160:161] op_sel_hi:[1,0]
	v_pk_mul_f32 v[2:3], v[2:3], v[160:161] op_sel_hi:[1,0]
	v_pk_mul_f32 v[0:1], v[0:1], v[160:161] op_sel_hi:[1,0]

.Lstg_b22:
	s_add_i32 s8, s85, -1
	s_cmp_ge_u32 s8, s75
	s_cselect_b64 s[66:67], -1, 0
	s_mov_b64 s[6:7], -1
	s_and_b64 vcc, exec, s[66:67]
	s_cbranch_vccz .LBB0_593
	v_mov_b32_e32 v144, s80
	ds_read_b32 v146, v144
	ds_read_b32 v144, v144 offset:4
	s_waitcnt vmcnt(0) lgkmcnt(0)
	v_readfirstlane_b32 s6, v146
	v_readfirstlane_b32 s7, v144
	s_nop 1
	s_nop 3
	s_mov_b32 m0, s78
	s_nop 0
	global_load_lds_dwordx4 v160, s[6:7]
	s_nop 3
	s_mov_b32 m0, s93
	s_nop 0
	global_load_lds_dwordx4 v170, s[6:7]
	s_mov_b64 s[6:7], 0

.Lstg_b23:
	s_cmp_gt_u32 s85, s75
	s_cbranch_scc1 .LBB0_604
	s_cmp_ge_u32 s85, s75
	s_mov_b64 s[6:7], -1
	s_cbranch_scc0 .LBB0_602
	v_mov_b32_e32 v148, s80
	ds_read_b32 v144, v148
	ds_read_b32 v147, v148 offset:4
	s_waitcnt vmcnt(0) lgkmcnt(0)
	v_readfirstlane_b32 s6, v144
	v_readfirstlane_b32 s7, v147
	s_nop 1
	s_nop 3
	s_mov_b32 m0, s78
	s_nop 0
	global_load_lds_dwordx4 v160, s[6:7]
	s_nop 3
	s_mov_b32 m0, s93
	s_nop 0
	global_load_lds_dwordx4 v170, s[6:7]
	s_mov_b64 s[6:7], 0

.LBB0_604:
	s_mov_b64 s[6:7], -1
	s_and_b64 vcc, exec, s[66:67]
	s_cbranch_vccz .LBB0_606
	v_mov_b32_e32 v148, s0
	ds_read_b32 v144, v148
	ds_read_b32 v147, v148 offset:4
	s_waitcnt vmcnt(0) lgkmcnt(0)
	v_readfirstlane_b32 s6, v144
	v_readfirstlane_b32 s7, v147
	s_nop 1
	s_nop 3
	s_mov_b32 m0, s3
	s_nop 0
	global_load_lds_dwordx4 v162, s[6:7]
	s_nop 3
	s_add_i32 m0, s69, 0xffffff80
	s_nop 0
	global_load_lds_dwordx4 v162, s[6:7] offset:128
	s_add_i32 m0, s68, 0xffffff00
	s_nop 0
	global_load_lds_dwordx4 v162, s[6:7] offset:256
	s_add_i32 m0, s2, 0xfffffe80
	s_nop 0
	global_load_lds_dwordx4 v162, s[6:7] offset:384
	s_mov_b64 s[6:7], 0

.Lstg_b24:
	v_mov_b32_e32 v146, s0
	ds_read_b32 v148, v146
	ds_read_b32 v146, v146 offset:4
	s_waitcnt vmcnt(0) lgkmcnt(0)
	v_readfirstlane_b32 s4, v148
	v_readfirstlane_b32 s5, v146
	s_nop 1
	s_nop 3
	s_mov_b32 m0, s3
	s_nop 0
	global_load_lds_dwordx4 v162, s[4:5]
	s_nop 3
	s_add_i32 m0, s69, 0xffffff80
	s_nop 0
	global_load_lds_dwordx4 v162, s[4:5] offset:128
	s_add_i32 m0, s68, 0xffffff00
	s_nop 0
	global_load_lds_dwordx4 v162, s[4:5] offset:256
	s_add_i32 m0, s2, 0xfffffe80
	s_nop 0
	global_load_lds_dwordx4 v162, s[4:5] offset:384
	v_cmp_gt_f32_e32 vcc, 1.0, v160
	s_cbranch_vccz .LBB0_551
	v_pk_mul_f32 v[126:127], v[126:127], v[160:161] op_sel_hi:[1,0]
	v_pk_mul_f32 v[124:125], v[124:125], v[160:161] op_sel_hi:[1,0]
	v_pk_mul_f32 v[122:123], v[122:123], v[160:161] op_sel_hi:[1,0]
	v_pk_mul_f32 v[120:121], v[120:121], v[160:161] op_sel_hi:[1,0]
	v_pk_mul_f32 v[118:119], v[118:119], v[160:161] op_sel_hi:[1,0]
	v_pk_mul_f32 v[116:117], v[116:117], v[160:161] op_sel_hi:[1,0]
	v_pk_mul_f32 v[114:115], v[114:115], v[160:161] op_sel_hi:[1,0]
	v_pk_mul_f32 v[112:113], v[112:113], v[160:161] op_sel_hi:[1,0]
	v_pk_mul_f32 v[110:111], v[110:111], v[160:161] op_sel_hi:[1,0]
	v_pk_mul_f32 v[108:109], v[108:109], v[160:161] op_sel_hi:[1,0]
	v_pk_mul_f32 v[106:107], v[106:107], v[160:161] op_sel_hi:[1,0]
	v_pk_mul_f32 v[104:105], v[104:105], v[160:161] op_sel_hi:[1,0]
	v_pk_mul_f32 v[102:103], v[102:103], v[160:161] op_sel_hi:[1,0]
	v_pk_mul_f32 v[100:101], v[100:101], v[160:161] op_sel_hi:[1,0]
	v_pk_mul_f32 v[98:99], v[98:99], v[160:161] op_sel_hi:[1,0]
	v_pk_mul_f32 v[96:97], v[96:97], v[160:161] op_sel_hi:[1,0]
	v_pk_mul_f32 v[94:95], v[94:95], v[160:161] op_sel_hi:[1,0]
	v_pk_mul_f32 v[92:93], v[92:93], v[160:161] op_sel_hi:[1,0]
	v_pk_mul_f32 v[90:91], v[90:91], v[160:161] op_sel_hi:[1,0]
	v_pk_mul_f32 v[88:89], v[88:89], v[160:161] op_sel_hi:[1,0]
	v_pk_mul_f32 v[86:87], v[86:87], v[160:161] op_sel_hi:[1,0]
	v_pk_mul_f32 v[84:85], v[84:85], v[160:161] op_sel_hi:[1,0]
	v_pk_mul_f32 v[82:83], v[82:83], v[160:161] op_sel_hi:[1,0]
	v_pk_mul_f32 v[80:81], v[80:81], v[160:161] op_sel_hi:[1,0]
	v_pk_mul_f32 v[78:79], v[78:79], v[160:161] op_sel_hi:[1,0]
	v_pk_mul_f32 v[76:77], v[76:77], v[160:161] op_sel_hi:[1,0]
	v_pk_mul_f32 v[74:75], v[74:75], v[160:161] op_sel_hi:[1,0]
	v_pk_mul_f32 v[72:73], v[72:73], v[160:161] op_sel_hi:[1,0]
	v_pk_mul_f32 v[70:71], v[70:71], v[160:161] op_sel_hi:[1,0]
	v_pk_mul_f32 v[68:69], v[68:69], v[160:161] op_sel_hi:[1,0]
	v_pk_mul_f32 v[66:67], v[66:67], v[160:161] op_sel_hi:[1,0]
	v_pk_mul_f32 v[64:65], v[64:65], v[160:161] op_sel_hi:[1,0]
	v_pk_mul_f32 v[62:63], v[62:63], v[160:161] op_sel_hi:[1,0]
	v_pk_mul_f32 v[60:61], v[60:61], v[160:161] op_sel_hi:[1,0]
	v_pk_mul_f32 v[58:59], v[58:59], v[160:161] op_sel_hi:[1,0]
	v_pk_mul_f32 v[56:57], v[56:57], v[160:161] op_sel_hi:[1,0]
	v_pk_mul_f32 v[54:55], v[54:55], v[160:161] op_sel_hi:[1,0]
	v_pk_mul_f32 v[52:53], v[52:53], v[160:161] op_sel_hi:[1,0]
	v_pk_mul_f32 v[50:51], v[50:51], v[160:161] op_sel_hi:[1,0]
	v_pk_mul_f32 v[48:49], v[48:49], v[160:161] op_sel_hi:[1,0]
	v_pk_mul_f32 v[46:47], v[46:47], v[160:161] op_sel_hi:[1,0]
	v_pk_mul_f32 v[44:45], v[44:45], v[160:161] op_sel_hi:[1,0]
	v_pk_mul_f32 v[42:43], v[42:43], v[160:161] op_sel_hi:[1,0]
	v_pk_mul_f32 v[40:41], v[40:41], v[160:161] op_sel_hi:[1,0]
	v_pk_mul_f32 v[38:39], v[38:39], v[160:161] op_sel_hi:[1,0]
	v_pk_mul_f32 v[36:37], v[36:37], v[160:161] op_sel_hi:[1,0]
	v_pk_mul_f32 v[34:35], v[34:35], v[160:161] op_sel_hi:[1,0]
	v_pk_mul_f32 v[32:33], v[32:33], v[160:161] op_sel_hi:[1,0]
	v_pk_mul_f32 v[30:31], v[30:31], v[160:161] op_sel_hi:[1,0]
	v_pk_mul_f32 v[28:29], v[28:29], v[160:161] op_sel_hi:[1,0]
	v_pk_mul_f32 v[26:27], v[26:27], v[160:161] op_sel_hi:[1,0]
	v_pk_mul_f32 v[24:25], v[24:25], v[160:161] op_sel_hi:[1,0]
	v_pk_mul_f32 v[22:23], v[22:23], v[160:161] op_sel_hi:[1,0]
	v_pk_mul_f32 v[20:21], v[20:21], v[160:161] op_sel_hi:[1,0]
	v_pk_mul_f32 v[18:19], v[18:19], v[160:161] op_sel_hi:[1,0]
	v_pk_mul_f32 v[16:17], v[16:17], v[160:161] op_sel_hi:[1,0]
	v_pk_mul_f32 v[14:15], v[14:15], v[160:161] op_sel_hi:[1,0]
	v_pk_mul_f32 v[12:13], v[12:13], v[160:161] op_sel_hi:[1,0]
	v_pk_mul_f32 v[10:11], v[10:11], v[160:161] op_sel_hi:[1,0]
	v_pk_mul_f32 v[8:9], v[8:9], v[160:161] op_sel_hi:[1,0]
	v_pk_mul_f32 v[6:7], v[6:7], v[160:161] op_sel_hi:[1,0]
	v_pk_mul_f32 v[4:5], v[4:5], v[160:161] op_sel_hi:[1,0]
	v_pk_mul_f32 v[2:3], v[2:3], v[160:161] op_sel_hi:[1,0]
	v_pk_mul_f32 v[0:1], v[0:1], v[160:161] op_sel_hi:[1,0]
	s_branch .LBB0_551
